# routed down GEMM: C=0 on first MFMA per accumulator, 2^-5 output scale folded into MFMA block scale (plus earlier barrier/rowpass edits)
# speedup vs baseline: 1.0299x; 1.0057x over previous
; #define PG8_STAGE(bufoff, gbase, voff) do { _Pragma("unroll") for (int _i = 0; _i < 2; ++_i) \
;         __builtin_amdgcn_global_load_lds((const unsigned*)((const char*)(gbase) + (voff)[_i]), (PG8_LAS unsigned*)(lds + (bufoff) + ldsw + _i * 8192), 16, 0, 0); } while (0)
; #define PG8_STAGE_A(bufoff, gbase, h, nx) do { if constexpr (Sched::GATHER) { unsigned _v[2]; _Pragma("unroll") for (int _i = 0; _i < 2; ++_i) _v[_i] = (nx) ? vAn[h][_i] : vA[h][_i]; PG8_STAGE(bufoff, gbase, _v); } \
;         else { PG8_STAGE(bufoff, (gbase) + (h) * hstep, voffA); } } while (0)
; #define PG8_WAIT_V(n) asm volatile("s_waitcnt vmcnt(" #n ")" ::: "memory")
; #define PG8_BAR __builtin_amdgcn_s_barrier()
; template <class Epi, class Sched, bool ALIGN_EPI = false, bool SP2 = false, bool FP8 = false>
; __device__ __forceinline__ void gemm_phase(PG8_LAS unsigned char* lds, const Gemm g, const Sched& S, const Epi& E) {
;     ...
;         PG8_STAGE(PG8_SB(0, 0), cB, voffB); PG8_STAGE(PG8_SB(0, 1), cB + hstep, voffB); PG8_STAGE_A(PG8_SA(0, 0), cA, 0, false); PG8_STAGE_A(PG8_SA(0, 1), cA, 1, false);
;         if (wr == 1) PG8_BAR;
;         PG8_WAIT_V(2); PG8_BAR;
;         PG8_STAGE(PG8_SB(1, 0), cB + kstep, voffB); PG8_STAGE_A(PG8_SA(1, 0), cA + kstep, 0, false); PG8_STAGE(PG8_SB(1, 1), cB + hstep + kstep, voffB);
;         PG8_WAIT_V(6); PG8_BAR;
;     __device__ __forceinline__ void operator()(const f32x4 (&acc)[2][2][4][2], const Unit& u, int wr, int wc, int fr, int fq) const {
;         const int lane = fq * 16 + fr, frs = lane >> 2, fqs = lane & 3;
;         const int r0 = wr * 64 + frs, col0 = (u.pn & 3) * 256 + wc * 64 + 16 * fqs;
.LBB0_1337:
	s_add_u32 s12, s18, 0x3c600000
	s_addc_u32 s13, s19, 0
	s_and_b32 s9, s20, 3
	s_add_i32 m0, s41, 0x18000
	v_lshl_add_u64 v[2:3], v[2:3], 0, s[88:89]
	s_lshl_b32 s23, s22, 13
	s_lshl_b32 s24, s9, 12
	s_waitcnt vmcnt(2)
	s_barrier
	global_load_lds_dwordx4 v[2:3], off
	s_add_i32 m0, s41, 0x1a000
	s_add_u32 s20, s18, 0x59a00080
	v_mov_b32_e32 v135, v163
	v_lshl_add_u64 v[2:3], v[4:5], 0, s[88:89]
	s_addc_u32 s21, s19, 0
	s_add_i32 s45, s41, 0x8000
	s_add_i32 s46, s41, 0xa000
	v_mov_b32_e32 v137, v163
	global_load_lds_dwordx4 v[2:3], off
	v_lshl_add_u64 v[2:3], s[20:21], 0, v[134:135]
	s_mov_b32 m0, s45
	s_add_u32 s18, s34, 0x8080
	global_load_lds_dwordx4 v[2:3], off
	v_lshl_add_u64 v[2:3], s[20:21], 0, v[136:137]
	s_mov_b32 m0, s46
	s_addc_u32 s19, s35, 0
	global_load_lds_dwordx4 v[2:3], off
	s_add_i32 m0, s41, 0x1c000
	v_lshl_add_u64 v[2:3], s[18:19], 0, v[130:131]
	global_load_lds_dwordx4 v[2:3], off
	v_lshl_add_u64 v[2:3], s[18:19], 0, v[132:133]
	s_add_i32 m0, s41, 0x1e000
	s_movk_i32 s18, 0x3c0
	global_load_lds_dwordx4 v[2:3], off
	v_and_b32_e32 v2, 48, v8
	v_lshlrev_b32_e32 v3, 6, v8
	v_lshlrev_b32_e32 v4, 2, v8
	v_and_or_b32 v2, v3, s18, v2
	v_and_b32_e32 v4, 32, v4
	v_bitop3_b32 v5, v2, s23, v4 bitop3:0xde
	v_bitop3_b32 v135, v2, s24, v4 bitop3:0xde
	v_bfe_u32 v2, v8, 2, 4
	s_waitcnt vmcnt(6)
	v_lshl_or_b32 v137, s22, 6, v2
	v_and_b32_e32 v2, 48, v9
	s_cmpk_lt_u32 s28, 0x100
	v_lshl_or_b32 v143, s9, 6, v2
	v_and_b32_e32 v2, 60, v8
	s_movk_i32 s9, 0xc0
	v_or_b32_e32 v145, 16, v137
	v_or_b32_e32 v146, 32, v137
	v_or_b32_e32 v147, 48, v137
	v_add_u32_e32 v148, 0x80, v137
	v_add_u32_e32 v149, 0x90, v137
	v_add_u32_e32 v150, 0xa0, v137
	v_add_u32_e32 v151, 0xb0, v137
	s_movk_i32 s47, 0x100
	s_cselect_b64 s[28:29], -1, 0
	v_and_or_b32 v144, v3, s9, v2
	v_lshl_add_u32 v152, v137, 2, s70
	v_lshl_add_u32 v153, v145, 2, s70
	v_lshl_add_u32 v154, v146, 2, s70
	v_lshl_add_u32 v155, v147, 2, s70
	v_lshl_add_u32 v156, v148, 2, s70
	v_lshl_add_u32 v157, v149, 2, s70
	v_lshl_add_u32 v158, v150, 2, s70
	v_lshl_add_u32 v159, v151, 2, s70
	s_mov_b32 s54, 0
	s_mov_b32 s48, 1
	v_add_u32_e32 v160, 0, v5
	v_readlane_b32 s49, v255, 19
	s_barrier
	v_mov_b32_e32 v240, 0x7a7a7a7a
	s_branch .LBB0_1340

; #define PG8_STAGE(bufoff, gbase, voff) do { _Pragma("unroll") for (int _i = 0; _i < 2; ++_i) \
;         __builtin_amdgcn_global_load_lds((const unsigned*)((const char*)(gbase) + (voff)[_i]), (PG8_LAS unsigned*)(lds + (bufoff) + ldsw + _i * 8192), 16, 0, 0); } while (0)
; #define PG8_STAGE_A(bufoff, gbase, h, nx) do { if constexpr (Sched::GATHER) { unsigned _v[2]; _Pragma("unroll") for (int _i = 0; _i < 2; ++_i) _v[_i] = (nx) ? vAn[h][_i] : vA[h][_i]; PG8_STAGE(bufoff, gbase, _v); } \
;         else { PG8_STAGE(bufoff, (gbase) + (h) * hstep, voffA); } } while (0)
; #define PG8_LDA(dst, b, h) do { _Pragma("unroll") for (int m = 0; m < 4; ++m) _Pragma("unroll") for (int k = 0; k < 2; ++k) dst[m][k] = *(const PG8_LAS bf16x8*)(lds + PG8_SA(b, h) + aoff + m * 2048 + k * 1024); } while (0)
; #define PG8_LDB(dst, b, h) do { _Pragma("unroll") for (int n = 0; n < 2; ++n) _Pragma("unroll") for (int k = 0; k < 2; ++k) dst[n][k] = *(const PG8_LAS bf16x8*)(lds + PG8_SB(b, h) + boff + n * 2048 + k * 1024); } while (0)
; #define PG8_WAIT_V(n) asm volatile("s_waitcnt vmcnt(" #n ")" ::: "memory")
; #define PG8_WAIT_L(n) asm volatile("s_waitcnt lgkmcnt(" #n ")" ::: "memory")
; #define PG8_BAR __builtin_amdgcn_s_barrier()
; #define PG8_SCHED __builtin_amdgcn_sched_barrier(0)
; template <class Epi, class Sched, bool ALIGN_EPI = false, bool SP2 = false, bool FP8 = false>
; __device__ __forceinline__ void gemm_phase(PG8_LAS unsigned char* lds, const Gemm g, const Sched& S, const Epi& E) {
;     ...
;             PG8_LDB(B0, 0, 0); PG8_LDB(B1, 0, 1); PG8_SCHED; PG8_LDA(At, 0, 0); PG8_STAGE_A(PG8_SA(1, 1), a1, 1, false);
;             PG8_WAIT_V(8); PG8_WAIT_L(0); PG8_BAR; PG8_MMA(0, 0, At, B0); PG8_MMA(0, 1, At, B1); PG8_BAR; PG8_SCHED;
;             PG8_LDA(At, 0, 1); PG8_STAGE(PG8_SB(0, 0), b2, voffB); PG8_STAGE(PG8_SB(0, 1), b2 + hstep, voffB); PG8_STAGE_A(PG8_SA(0, 0), a2, 0, last);
;             PG8_WAIT_V(8); PG8_WAIT_L(0); PG8_BAR; PG8_MMA(1, 0, At, B0); PG8_MMA(1, 1, At, B1); PG8_BAR; PG8_SCHED;
.LBB0_1344:
	s_ashr_i32 s31, s30, 31
	s_lshl_b64 s[22:23], s[30:31], 16
	s_add_u32 s38, s11, s22
	s_addc_u32 s39, s16, s23
	s_and_b64 s[18:19], s[18:19], exec
	s_cselect_b32 s18, s38, s34
	s_cselect_b32 s19, s39, s35
	s_add_u32 s34, s18, 0x8000
	s_addc_u32 s35, s19, 0
	s_add_i32 s9, 0, 0x10000
	s_waitcnt lgkmcnt(0)
	v_add_u32_e32 v2, s9, v135
	s_add_i32 s22, 0, 0x14000
	ds_read_b128 v[26:29], v2
	ds_read_b128 v[30:33], v2 offset:1024
	ds_read_b128 v[42:45], v2 offset:2048
	ds_read_b128 v[46:49], v2 offset:3072
	v_add_u32_e32 v2, s22, v135
	ds_read_b128 v[170:173], v2
	ds_read_b128 v[174:177], v2 offset:1024
	ds_read_b128 v[178:181], v2 offset:2048
	ds_read_b128 v[182:185], v2 offset:3072
	s_add_i32 m0, s41, 0xc000
	ds_read_b128 v[8:11], v160
	ds_read_b128 v[12:15], v160 offset:1024
	ds_read_b128 v[16:19], v160 offset:2048
	ds_read_b128 v[20:23], v160 offset:3072
	ds_read_b128 v[34:37], v160 offset:4096
	ds_read_b128 v[38:41], v160 offset:5120
	ds_read_b128 v[58:61], v160 offset:6144
	ds_read_b128 v[62:65], v160 offset:7168
	global_load_lds_dwordx4 v7, s[20:21]
	s_add_i32 m0, s41, 0xe000
	s_nop 0
	global_load_lds_dwordx4 v6, s[20:21]
	s_waitcnt vmcnt(8)
	s_waitcnt lgkmcnt(0)
	s_barrier
	s_setprio 1
	v_readlane_b32 s60, v255, 1
	v_readlane_b32 s61, v255, 2
	v_readlane_b32 s62, v255, 3
	v_readlane_b32 s63, v255, 4
	s_waitcnt lgkmcnt(0)
	v_mfma_scale_f32_16x16x128_f8f6f4 v[114:117], v[26:33], v[8:15], 0, v240, v199 op_sel_hi:[0,0,0]
	v_mfma_scale_f32_16x16x128_f8f6f4 v[118:121], v[42:49], v[8:15], 0, v240, v199 op_sel_hi:[0,0,0]
	v_mfma_scale_f32_16x16x128_f8f6f4 v[102:105], v[26:33], v[16:23], 0, v240, v199 op_sel_hi:[0,0,0]
	v_mfma_scale_f32_16x16x128_f8f6f4 v[98:101], v[42:49], v[16:23], 0, v240, v199 op_sel_hi:[0,0,0]
	v_mfma_scale_f32_16x16x128_f8f6f4 v[86:89], v[26:33], v[34:41], 0, v240, v199 op_sel_hi:[0,0,0]
	v_mfma_scale_f32_16x16x128_f8f6f4 v[82:85], v[42:49], v[34:41], 0, v240, v199 op_sel_hi:[0,0,0]
	v_mfma_scale_f32_16x16x128_f8f6f4 v[54:57], v[26:33], v[58:65], 0, v240, v199 op_sel_hi:[0,0,0]
	v_mfma_scale_f32_16x16x128_f8f6f4 v[50:53], v[42:49], v[58:65], 0, v240, v199 op_sel_hi:[0,0,0]
	s_setprio 0
	s_setprio 1
	v_mfma_scale_f32_16x16x128_f8f6f4 v[122:125], v[170:177], v[8:15], 0, v240, v199 op_sel_hi:[0,0,0]
	v_mfma_scale_f32_16x16x128_f8f6f4 v[126:129], v[178:185], v[8:15], 0, v240, v199 op_sel_hi:[0,0,0]
	v_mfma_scale_f32_16x16x128_f8f6f4 v[110:113], v[170:177], v[16:23], 0, v240, v199 op_sel_hi:[0,0,0]
	v_mfma_scale_f32_16x16x128_f8f6f4 v[106:109], v[178:185], v[16:23], 0, v240, v199 op_sel_hi:[0,0,0]
	v_mfma_scale_f32_16x16x128_f8f6f4 v[94:97], v[170:177], v[34:41], 0, v240, v199 op_sel_hi:[0,0,0]
	v_mfma_scale_f32_16x16x128_f8f6f4 v[90:93], v[178:185], v[34:41], 0, v240, v199 op_sel_hi:[0,0,0]
	v_mfma_scale_f32_16x16x128_f8f6f4 v[70:73], v[170:177], v[58:65], 0, v240, v199 op_sel_hi:[0,0,0]
	v_mfma_scale_f32_16x16x128_f8f6f4 v[66:69], v[178:185], v[58:65], 0, v240, v199 op_sel_hi:[0,0,0]
	s_setprio 0
	s_barrier
	s_add_i32 s9, s9, s5
	v_lshl_add_u64 v[138:139], s[18:19], 0, v[130:131]
	s_mov_b32 m0, s9
	ds_read_b128 v[186:189], v160 offset:16384
	ds_read_b128 v[190:193], v160 offset:17408
	ds_read_b128 v[200:203], v160 offset:18432
	ds_read_b128 v[204:207], v160 offset:19456
	ds_read_b128 v[208:211], v160 offset:20480
	ds_read_b128 v[212:215], v160 offset:21504
	ds_read_b128 v[216:219], v160 offset:22528
	ds_read_b128 v[220:223], v160 offset:23552
	global_load_lds_dwordx4 v[138:139], off
	v_lshl_add_u64 v[164:165], s[18:19], 0, v[132:133]
	s_add_i32 m0, s9, 0x2000
	s_add_i32 s9, s22, s5
	global_load_lds_dwordx4 v[164:165], off
	v_lshl_add_u64 v[6:7], s[34:35], 0, v[130:131]
	s_mov_b32 m0, s9
	s_nop 0
	global_load_lds_dwordx4 v[6:7], off
	v_lshl_add_u64 v[6:7], s[34:35], 0, v[132:133]
	s_add_i32 m0, s9, 0x2000
	s_nop 0
	global_load_lds_dwordx4 v[6:7], off
	s_mov_b32 m0, s41
	s_nop 0
	global_load_lds_dwordx4 v134, s[0:1]
	s_mov_b32 m0, s42
	s_nop 0
	global_load_lds_dwordx4 v136, s[0:1]
	s_waitcnt vmcnt(8)
	s_waitcnt lgkmcnt(0)
	s_barrier
	s_setprio 1
	s_waitcnt lgkmcnt(0)
	v_mfma_scale_f32_16x16x128_f8f6f4 v[62:65], v[26:33], v[186:193], 0, v240, v199 op_sel_hi:[0,0,0]
	v_mfma_scale_f32_16x16x128_f8f6f4 v[58:61], v[42:49], v[186:193], 0, v240, v199 op_sel_hi:[0,0,0]
	v_mfma_scale_f32_16x16x128_f8f6f4 v[38:41], v[26:33], v[200:207], 0, v240, v199 op_sel_hi:[0,0,0]
	v_mfma_scale_f32_16x16x128_f8f6f4 v[34:37], v[42:49], v[200:207], 0, v240, v199 op_sel_hi:[0,0,0]
	v_mfma_scale_f32_16x16x128_f8f6f4 v[22:25], v[26:33], v[208:215], 0, v240, v199 op_sel_hi:[0,0,0]
	v_mfma_scale_f32_16x16x128_f8f6f4 v[18:21], v[42:49], v[208:215], 0, v240, v199 op_sel_hi:[0,0,0]
	v_mfma_scale_f32_16x16x128_f8f6f4 v[10:13], v[26:33], v[216:223], 0, v240, v199 op_sel_hi:[0,0,0]
	v_mfma_scale_f32_16x16x128_f8f6f4 v[6:9], v[42:49], v[216:223], 0, v240, v199 op_sel_hi:[0,0,0]
	s_setprio 0
	s_setprio 1
	v_mfma_scale_f32_16x16x128_f8f6f4 v[78:81], v[170:177], v[186:193], 0, v240, v199 op_sel_hi:[0,0,0]
	v_mfma_scale_f32_16x16x128_f8f6f4 v[74:77], v[178:185], v[186:193], 0, v240, v199 op_sel_hi:[0,0,0]
	v_mfma_scale_f32_16x16x128_f8f6f4 v[46:49], v[170:177], v[200:207], 0, v240, v199 op_sel_hi:[0,0,0]
	v_mfma_scale_f32_16x16x128_f8f6f4 v[42:45], v[178:185], v[200:207], 0, v240, v199 op_sel_hi:[0,0,0]
	v_mfma_scale_f32_16x16x128_f8f6f4 v[30:33], v[170:177], v[208:215], 0, v240, v199 op_sel_hi:[0,0,0]
	v_mfma_scale_f32_16x16x128_f8f6f4 v[26:29], v[178:185], v[208:215], 0, v240, v199 op_sel_hi:[0,0,0]
	v_mfma_scale_f32_16x16x128_f8f6f4 v[14:17], v[170:177], v[216:223], 0, v240, v199 op_sel_hi:[0,0,0]
	v_mfma_scale_f32_16x16x128_f8f6f4 v[2:5], v[178:185], v[216:223], 0, v240, v199 op_sel_hi:[0,0,0]
	s_setprio 0
	s_barrier
; #define PG8_STAGE(bufoff, gbase, voff) do { _Pragma("unroll") for (int _i = 0; _i < 2; ++_i) \
;         __builtin_amdgcn_global_load_lds((const unsigned*)((const char*)(gbase) + (voff)[_i]), (PG8_LAS unsigned*)(lds + (bufoff) + ldsw + _i * 8192), 16, 0, 0); } while (0)
; #define PG8_STAGE_A(bufoff, gbase, h, nx) do { if constexpr (Sched::GATHER) { unsigned _v[2]; _Pragma("unroll") for (int _i = 0; _i < 2; ++_i) _v[_i] = (nx) ? vAn[h][_i] : vA[h][_i]; PG8_STAGE(bufoff, gbase, _v); } \
;         else { PG8_STAGE(bufoff, (gbase) + (h) * hstep, voffA); } } while (0)
; #define PG8_LDA(dst, b, h) do { _Pragma("unroll") for (int m = 0; m < 4; ++m) _Pragma("unroll") for (int k = 0; k < 2; ++k) dst[m][k] = *(const PG8_LAS bf16x8*)(lds + PG8_SA(b, h) + aoff + m * 2048 + k * 1024); } while (0)
; #define PG8_LDB(dst, b, h) do { _Pragma("unroll") for (int n = 0; n < 2; ++n) _Pragma("unroll") for (int k = 0; k < 2; ++k) dst[n][k] = *(const PG8_LAS bf16x8*)(lds + PG8_SB(b, h) + boff + n * 2048 + k * 1024); } while (0)
; #define PG8_WAIT_V(n) asm volatile("s_waitcnt vmcnt(" #n ")" ::: "memory")
; #define PG8_WAIT_L(n) asm volatile("s_waitcnt lgkmcnt(" #n ")" ::: "memory")
; #define PG8_BAR __builtin_amdgcn_s_barrier()
; #define PG8_SCHED __builtin_amdgcn_sched_barrier(0)
; template <class Epi, class Sched, bool ALIGN_EPI = false, bool SP2 = false, bool FP8 = false>
; __device__ __forceinline__ void gemm_phase(PG8_LAS unsigned char* lds, const Gemm g, const Sched& S, const Epi& E) {
;     ...
;             PG8_LDB(B0, 1, 0); PG8_LDB(B1, 1, 1); PG8_SCHED; PG8_LDA(At, 1, 0); PG8_STAGE_A(PG8_SA(0, 1), a2, 1, last);
;             PG8_WAIT_V(8); PG8_WAIT_L(0); PG8_BAR; PG8_MMA(0, 0, At, B0); PG8_MMA(0, 1, At, B1); PG8_BAR; PG8_SCHED;
;             PG8_LDA(At, 1, 1); PG8_STAGE(PG8_SB(1, 0), b3, voffB); PG8_STAGE(PG8_SB(1, 1), b3 + hstep, voffB); PG8_STAGE_A(PG8_SA(1, 0), a3, 0, last);
;             PG8_WAIT_V(8); PG8_WAIT_L(0); PG8_BAR; PG8_MMA(1, 0, At, B0); PG8_MMA(1, 1, At, B1); PG8_BAR; PG8_SCHED;
;     ...
;         if constexpr (ALIGN_EPI) { if (wr == 0) PG8_BAR; }
	s_add_i32 s9, 0, 0x18000
	v_add_u32_e32 v162, s9, v135
	s_add_i32 s22, 0, 0x1c000
	ds_read_b128 v[170:173], v162
	ds_read_b128 v[174:177], v162 offset:1024
	ds_read_b128 v[178:181], v162 offset:2048
	ds_read_b128 v[182:185], v162 offset:3072
	v_add_u32_e32 v162, s22, v135
	ds_read_b128 v[186:189], v162
	ds_read_b128 v[190:193], v162 offset:1024
	ds_read_b128 v[200:203], v162 offset:2048
	ds_read_b128 v[204:207], v162 offset:3072
	s_mov_b32 m0, s43
	ds_read_b128 v[208:211], v160 offset:32768
	ds_read_b128 v[212:215], v160 offset:33792
	ds_read_b128 v[216:219], v160 offset:34816
	ds_read_b128 v[220:223], v160 offset:35840
	ds_read_b128 v[224:227], v160 offset:36864
	ds_read_b128 v[228:231], v160 offset:37888
	ds_read_b128 v[232:235], v160 offset:38912
	ds_read_b128 v[236:239], v160 offset:39936
	global_load_lds_dwordx4 v161, s[0:1]
	s_mov_b32 m0, s44
	s_nop 0
	global_load_lds_dwordx4 v168, s[0:1]
	s_waitcnt vmcnt(8)
	s_waitcnt lgkmcnt(0)
	s_barrier
	s_setprio 1
	s_waitcnt lgkmcnt(0)
	v_mfma_scale_f32_16x16x128_f8f6f4 v[114:117], v[170:177], v[208:215], v[114:117], v240, v199 op_sel_hi:[0,0,0]
	v_mfma_scale_f32_16x16x128_f8f6f4 v[118:121], v[178:185], v[208:215], v[118:121], v240, v199 op_sel_hi:[0,0,0]
	v_mfma_scale_f32_16x16x128_f8f6f4 v[102:105], v[170:177], v[216:223], v[102:105], v240, v199 op_sel_hi:[0,0,0]
	v_mfma_scale_f32_16x16x128_f8f6f4 v[98:101], v[178:185], v[216:223], v[98:101], v240, v199 op_sel_hi:[0,0,0]
	v_mfma_scale_f32_16x16x128_f8f6f4 v[86:89], v[170:177], v[224:231], v[86:89], v240, v199 op_sel_hi:[0,0,0]
	v_mfma_scale_f32_16x16x128_f8f6f4 v[82:85], v[178:185], v[224:231], v[82:85], v240, v199 op_sel_hi:[0,0,0]
	v_mfma_scale_f32_16x16x128_f8f6f4 v[54:57], v[170:177], v[232:239], v[54:57], v240, v199 op_sel_hi:[0,0,0]
	v_mfma_scale_f32_16x16x128_f8f6f4 v[50:53], v[178:185], v[232:239], v[50:53], v240, v199 op_sel_hi:[0,0,0]
	s_setprio 0
	s_setprio 1
	v_mfma_scale_f32_16x16x128_f8f6f4 v[122:125], v[186:193], v[208:215], v[122:125], v240, v199 op_sel_hi:[0,0,0]
	v_mfma_scale_f32_16x16x128_f8f6f4 v[126:129], v[200:207], v[208:215], v[126:129], v240, v199 op_sel_hi:[0,0,0]
	v_mfma_scale_f32_16x16x128_f8f6f4 v[110:113], v[186:193], v[216:223], v[110:113], v240, v199 op_sel_hi:[0,0,0]
	v_mfma_scale_f32_16x16x128_f8f6f4 v[106:109], v[200:207], v[216:223], v[106:109], v240, v199 op_sel_hi:[0,0,0]
	v_mfma_scale_f32_16x16x128_f8f6f4 v[94:97], v[186:193], v[224:231], v[94:97], v240, v199 op_sel_hi:[0,0,0]
	v_mfma_scale_f32_16x16x128_f8f6f4 v[90:93], v[200:207], v[224:231], v[90:93], v240, v199 op_sel_hi:[0,0,0]
	v_mfma_scale_f32_16x16x128_f8f6f4 v[70:73], v[186:193], v[232:239], v[70:73], v240, v199 op_sel_hi:[0,0,0]
	v_mfma_scale_f32_16x16x128_f8f6f4 v[66:69], v[200:207], v[232:239], v[66:69], v240, v199 op_sel_hi:[0,0,0]
	s_setprio 0
	s_barrier
	s_add_i32 s9, s9, s5
	v_lshl_add_u64 v[138:139], v[138:139], 0, s[88:89]
	s_mov_b32 m0, s9
	ds_read_b128 v[208:211], v160 offset:49152
	ds_read_b128 v[212:215], v160 offset:50176
	ds_read_b128 v[216:219], v160 offset:51200
	ds_read_b128 v[220:223], v160 offset:52224
	ds_read_b128 v[224:227], v160 offset:53248
	ds_read_b128 v[228:231], v160 offset:54272
	ds_read_b128 v[232:235], v160 offset:55296
	ds_read_b128 v[236:239], v160 offset:56320
	global_load_lds_dwordx4 v[138:139], off
	s_add_i32 m0, s9, 0x2000
	s_add_u32 s18, s18, 0x8080
	v_lshl_add_u64 v[138:139], v[164:165], 0, s[88:89]
	s_addc_u32 s19, s19, 0
	s_add_i32 s9, s22, s5
	global_load_lds_dwordx4 v[138:139], off
	v_lshl_add_u64 v[138:139], s[18:19], 0, v[130:131]
	s_mov_b32 m0, s9
	s_nop 0
	global_load_lds_dwordx4 v[138:139], off
	v_lshl_add_u64 v[138:139], s[18:19], 0, v[132:133]
	s_add_i32 m0, s9, 0x2000
	s_nop 0
	global_load_lds_dwordx4 v[138:139], off
	s_mov_b32 m0, s45
	s_nop 0
	global_load_lds_dwordx4 v134, s[20:21]
	s_mov_b32 m0, s46
	s_nop 0
	global_load_lds_dwordx4 v136, s[20:21]
	s_waitcnt vmcnt(8)
	s_waitcnt lgkmcnt(0)
	s_barrier
	s_setprio 1
	s_waitcnt lgkmcnt(0)
	v_mfma_scale_f32_16x16x128_f8f6f4 v[62:65], v[170:177], v[208:215], v[62:65], v240, v199 op_sel_hi:[0,0,0]
	v_mfma_scale_f32_16x16x128_f8f6f4 v[58:61], v[178:185], v[208:215], v[58:61], v240, v199 op_sel_hi:[0,0,0]
	v_mfma_scale_f32_16x16x128_f8f6f4 v[38:41], v[170:177], v[216:223], v[38:41], v240, v199 op_sel_hi:[0,0,0]
	v_mfma_scale_f32_16x16x128_f8f6f4 v[34:37], v[178:185], v[216:223], v[34:37], v240, v199 op_sel_hi:[0,0,0]
	v_mfma_scale_f32_16x16x128_f8f6f4 v[22:25], v[170:177], v[224:231], v[22:25], v240, v199 op_sel_hi:[0,0,0]
	v_mfma_scale_f32_16x16x128_f8f6f4 v[18:21], v[178:185], v[224:231], v[18:21], v240, v199 op_sel_hi:[0,0,0]
	v_mfma_scale_f32_16x16x128_f8f6f4 v[10:13], v[170:177], v[232:239], v[10:13], v240, v199 op_sel_hi:[0,0,0]
	v_mfma_scale_f32_16x16x128_f8f6f4 v[6:9], v[178:185], v[232:239], v[6:9], v240, v199 op_sel_hi:[0,0,0]
	s_setprio 0
	s_setprio 1
	v_mfma_scale_f32_16x16x128_f8f6f4 v[78:81], v[186:193], v[208:215], v[78:81], v240, v199 op_sel_hi:[0,0,0]
	v_mfma_scale_f32_16x16x128_f8f6f4 v[74:77], v[200:207], v[208:215], v[74:77], v240, v199 op_sel_hi:[0,0,0]
	v_mfma_scale_f32_16x16x128_f8f6f4 v[46:49], v[186:193], v[216:223], v[46:49], v240, v199 op_sel_hi:[0,0,0]
	v_mfma_scale_f32_16x16x128_f8f6f4 v[42:45], v[200:207], v[216:223], v[42:45], v240, v199 op_sel_hi:[0,0,0]
	v_mfma_scale_f32_16x16x128_f8f6f4 v[30:33], v[186:193], v[224:231], v[30:33], v240, v199 op_sel_hi:[0,0,0]
	v_mfma_scale_f32_16x16x128_f8f6f4 v[26:29], v[200:207], v[224:231], v[26:29], v240, v199 op_sel_hi:[0,0,0]
	v_mfma_scale_f32_16x16x128_f8f6f4 v[14:17], v[186:193], v[232:239], v[14:17], v240, v199 op_sel_hi:[0,0,0]
	v_mfma_scale_f32_16x16x128_f8f6f4 v[2:5], v[200:207], v[232:239], v[2:5], v240, v199 op_sel_hi:[0,0,0]
	s_setprio 0
	s_barrier
	s_andn2_b64 vcc, exec, s[28:29]
	s_cbranch_vccnz .LBB0_1346
	s_barrier

;     __device__ __forceinline__ void operator()(const f32x4 (&acc)[2][2][4][2], const Unit& u, int wr, int wc, int fr, int fq) const {
;     ...
;             for (int m = 0; m < 4; ++m) { const int r = r0 + ai * 128 + m * 16; const bool ok = r < u.aux1; const int pid = ok ? list[u.aux0 + r] : 0;
;                 v4u w;
;                 { const f32x4 a0 = acc[ai][0][m][0] * sc, a1 = acc[ai][0][m][1] * sc, a2 = acc[ai][1][m][0] * sc, a3 = acc[ai][1][m][1] * sc;
;                   w.x = (unsigned)__builtin_amdgcn_cvt_pk_fp8_f32(a0[2], a0[3], __builtin_amdgcn_cvt_pk_fp8_f32(a0[0], a0[1], 0, false), true);
;                   w.y = (unsigned)__builtin_amdgcn_cvt_pk_fp8_f32(a1[2], a1[3], __builtin_amdgcn_cvt_pk_fp8_f32(a1[0], a1[1], 0, false), true);
;                   w.z = (unsigned)__builtin_amdgcn_cvt_pk_fp8_f32(a2[2], a2[3], __builtin_amdgcn_cvt_pk_fp8_f32(a2[0], a2[1], 0, false), true);
;                   w.w = (unsigned)__builtin_amdgcn_cvt_pk_fp8_f32(a3[2], a3[3], __builtin_amdgcn_cvt_pk_fp8_f32(a3[0], a3[1], 0, false), true); }
;                 w = lane_xpose(w, lane);
;                 if (ok) *(v4u*)(Y + (size_t)pid * 1024 + col0) = w; }
.LBB0_1348:
	s_or_b64 exec, exec, s[18:19]
	v_mov_b32_e32 v162, v163
	v_cvt_pk_fp8_f32 v162, v114, v115
	v_mov_b32_e32 v115, v163
	v_cvt_pk_fp8_f32 v115, v118, v119
	v_mov_b32_e32 v118, v163
	v_mov_b32_e32 v119, v163
	v_cvt_pk_fp8_f32 v118, v122, v123
	v_cvt_pk_fp8_f32 v119, v126, v127
	v_cvt_pk_fp8_f32 v162, v116, v117 op_sel:[0,0,1]
	v_cvt_pk_fp8_f32 v115, v120, v121 op_sel:[0,0,1]
	v_cvt_pk_fp8_f32 v118, v124, v125 op_sel:[0,0,1]
	v_cvt_pk_fp8_f32 v119, v128, v129 op_sel:[0,0,1]
	ds_bpermute_b32 v114, v144, v162
	ds_bpermute_b32 v115, v144, v115
	ds_bpermute_b32 v116, v144, v118
	ds_bpermute_b32 v117, v144, v119
	s_lshl_b32 s8, s8, 8
	s_and_b32 s8, s8, 0x300
	v_or_b32_e32 v162, s8, v143
	s_and_saveexec_b64 s[8:9], vcc
	s_movk_i32 s63, 0x2440
	s_movk_i32 s62, 0x2000
	s_movk_i32 s61, 0xdff
	s_cbranch_execz .LBB0_1350
	v_lshl_add_u64 v[118:119], s[12:13], 0, v[138:139]
	v_lshl_add_u64 v[118:119], v[118:119], 0, v[162:163]
	s_waitcnt lgkmcnt(0)
	global_store_dwordx4 v[118:119], v[114:117], off

;     __device__ __forceinline__ void operator()(const f32x4 (&acc)[2][2][4][2], const Unit& u, int wr, int wc, int fr, int fq) const {
;     ...
;             for (int m = 0; m < 4; ++m) { const int r = r0 + ai * 128 + m * 16; const bool ok = r < u.aux1; const int pid = ok ? list[u.aux0 + r] : 0;
;                 v4u w;
;                 { const f32x4 a0 = acc[ai][0][m][0] * sc, a1 = acc[ai][0][m][1] * sc, a2 = acc[ai][1][m][0] * sc, a3 = acc[ai][1][m][1] * sc;
;                   w.x = (unsigned)__builtin_amdgcn_cvt_pk_fp8_f32(a0[2], a0[3], __builtin_amdgcn_cvt_pk_fp8_f32(a0[0], a0[1], 0, false), true);
;                   w.y = (unsigned)__builtin_amdgcn_cvt_pk_fp8_f32(a1[2], a1[3], __builtin_amdgcn_cvt_pk_fp8_f32(a1[0], a1[1], 0, false), true);
;                   w.z = (unsigned)__builtin_amdgcn_cvt_pk_fp8_f32(a2[2], a2[3], __builtin_amdgcn_cvt_pk_fp8_f32(a2[0], a2[1], 0, false), true);
;                   w.w = (unsigned)__builtin_amdgcn_cvt_pk_fp8_f32(a3[2], a3[3], __builtin_amdgcn_cvt_pk_fp8_f32(a3[0], a3[1], 0, false), true); }
;                 w = lane_xpose(w, lane);
;                 if (ok) *(v4u*)(Y + (size_t)pid * 1024 + col0) = w; }
.LBB0_1352:
	s_or_b64 exec, exec, s[8:9]
	v_mov_b32_e32 v116, v163
	v_cvt_pk_fp8_f32 v116, v102, v103
	v_mov_b32_e32 v103, v163
	v_mov_b32_e32 v102, v163
	v_cvt_pk_fp8_f32 v103, v110, v111
	v_mov_b32_e32 v110, v163
	v_cvt_pk_fp8_f32 v102, v98, v99
	v_cvt_pk_fp8_f32 v110, v106, v107
	v_cvt_pk_fp8_f32 v116, v104, v105 op_sel:[0,0,1]
	v_cvt_pk_fp8_f32 v102, v100, v101 op_sel:[0,0,1]
	v_cvt_pk_fp8_f32 v103, v112, v113 op_sel:[0,0,1]
	v_cvt_pk_fp8_f32 v110, v108, v109 op_sel:[0,0,1]
	ds_bpermute_b32 v98, v144, v116
	ds_bpermute_b32 v99, v144, v102
	ds_bpermute_b32 v100, v144, v103
	ds_bpermute_b32 v101, v144, v110
	s_and_saveexec_b64 s[8:9], vcc
	s_cbranch_execz .LBB0_1354
	v_lshl_add_u64 v[102:103], s[12:13], 0, v[114:115]
	v_lshl_add_u64 v[102:103], v[102:103], 0, v[162:163]
	s_waitcnt lgkmcnt(0)
	global_store_dwordx4 v[102:103], v[98:101], off

;     __device__ __forceinline__ void operator()(const f32x4 (&acc)[2][2][4][2], const Unit& u, int wr, int wc, int fr, int fq) const {
;     ...
;             for (int m = 0; m < 4; ++m) { const int r = r0 + ai * 128 + m * 16; const bool ok = r < u.aux1; const int pid = ok ? list[u.aux0 + r] : 0;
;                 v4u w;
;                 { const f32x4 a0 = acc[ai][0][m][0] * sc, a1 = acc[ai][0][m][1] * sc, a2 = acc[ai][1][m][0] * sc, a3 = acc[ai][1][m][1] * sc;
;                   w.x = (unsigned)__builtin_amdgcn_cvt_pk_fp8_f32(a0[2], a0[3], __builtin_amdgcn_cvt_pk_fp8_f32(a0[0], a0[1], 0, false), true);
;                   w.y = (unsigned)__builtin_amdgcn_cvt_pk_fp8_f32(a1[2], a1[3], __builtin_amdgcn_cvt_pk_fp8_f32(a1[0], a1[1], 0, false), true);
;                   w.z = (unsigned)__builtin_amdgcn_cvt_pk_fp8_f32(a2[2], a2[3], __builtin_amdgcn_cvt_pk_fp8_f32(a2[0], a2[1], 0, false), true);
;                   w.w = (unsigned)__builtin_amdgcn_cvt_pk_fp8_f32(a3[2], a3[3], __builtin_amdgcn_cvt_pk_fp8_f32(a3[0], a3[1], 0, false), true); }
;                 w = lane_xpose(w, lane);
;                 if (ok) *(v4u*)(Y + (size_t)pid * 1024 + col0) = w; }
.LBB0_1356:
	s_or_b64 exec, exec, s[8:9]
	v_mov_b32_e32 v100, v163
	v_cvt_pk_fp8_f32 v100, v86, v87
	v_mov_b32_e32 v87, v163
	v_mov_b32_e32 v86, v163
	v_cvt_pk_fp8_f32 v87, v94, v95
	v_mov_b32_e32 v94, v163
	v_cvt_pk_fp8_f32 v86, v82, v83
	v_cvt_pk_fp8_f32 v94, v90, v91
	v_cvt_pk_fp8_f32 v100, v88, v89 op_sel:[0,0,1]
	v_cvt_pk_fp8_f32 v86, v84, v85 op_sel:[0,0,1]
	v_cvt_pk_fp8_f32 v87, v96, v97 op_sel:[0,0,1]
	v_cvt_pk_fp8_f32 v94, v92, v93 op_sel:[0,0,1]
	ds_bpermute_b32 v82, v144, v100
	ds_bpermute_b32 v83, v144, v86
	ds_bpermute_b32 v84, v144, v87
	ds_bpermute_b32 v85, v144, v94
	s_and_saveexec_b64 s[8:9], vcc
	s_cbranch_execz .LBB0_1358
	v_lshl_add_u64 v[86:87], s[12:13], 0, v[98:99]
	v_lshl_add_u64 v[86:87], v[86:87], 0, v[162:163]
	s_waitcnt lgkmcnt(0)
	global_store_dwordx4 v[86:87], v[82:85], off

;     __device__ __forceinline__ void operator()(const f32x4 (&acc)[2][2][4][2], const Unit& u, int wr, int wc, int fr, int fq) const {
;     ...
;             for (int m = 0; m < 4; ++m) { const int r = r0 + ai * 128 + m * 16; const bool ok = r < u.aux1; const int pid = ok ? list[u.aux0 + r] : 0;
;                 v4u w;
;                 { const f32x4 a0 = acc[ai][0][m][0] * sc, a1 = acc[ai][0][m][1] * sc, a2 = acc[ai][1][m][0] * sc, a3 = acc[ai][1][m][1] * sc;
;                   w.x = (unsigned)__builtin_amdgcn_cvt_pk_fp8_f32(a0[2], a0[3], __builtin_amdgcn_cvt_pk_fp8_f32(a0[0], a0[1], 0, false), true);
;                   w.y = (unsigned)__builtin_amdgcn_cvt_pk_fp8_f32(a1[2], a1[3], __builtin_amdgcn_cvt_pk_fp8_f32(a1[0], a1[1], 0, false), true);
;                   w.z = (unsigned)__builtin_amdgcn_cvt_pk_fp8_f32(a2[2], a2[3], __builtin_amdgcn_cvt_pk_fp8_f32(a2[0], a2[1], 0, false), true);
;                   w.w = (unsigned)__builtin_amdgcn_cvt_pk_fp8_f32(a3[2], a3[3], __builtin_amdgcn_cvt_pk_fp8_f32(a3[0], a3[1], 0, false), true); }
;                 w = lane_xpose(w, lane);
;                 if (ok) *(v4u*)(Y + (size_t)pid * 1024 + col0) = w; }
.LBB0_1360:
	s_or_b64 exec, exec, s[8:9]
	v_mov_b32_e32 v84, v163
	v_cvt_pk_fp8_f32 v84, v54, v55
	v_mov_b32_e32 v55, v163
	v_mov_b32_e32 v54, v163
	v_cvt_pk_fp8_f32 v55, v70, v71
	v_mov_b32_e32 v70, v163
	v_cvt_pk_fp8_f32 v54, v50, v51
	v_cvt_pk_fp8_f32 v70, v66, v67
	v_cvt_pk_fp8_f32 v84, v56, v57 op_sel:[0,0,1]
	v_cvt_pk_fp8_f32 v54, v52, v53 op_sel:[0,0,1]
	v_cvt_pk_fp8_f32 v55, v72, v73 op_sel:[0,0,1]
	v_cvt_pk_fp8_f32 v70, v68, v69 op_sel:[0,0,1]
	ds_bpermute_b32 v50, v144, v84
	ds_bpermute_b32 v51, v144, v54
	ds_bpermute_b32 v52, v144, v55
	ds_bpermute_b32 v53, v144, v70
	s_and_saveexec_b64 s[8:9], vcc
	s_cbranch_execz .LBB0_1362
	v_lshl_add_u64 v[54:55], s[12:13], 0, v[82:83]
	v_lshl_add_u64 v[54:55], v[54:55], 0, v[162:163]
	s_waitcnt lgkmcnt(0)
	global_store_dwordx4 v[54:55], v[50:53], off

;     __device__ __forceinline__ void operator()(const f32x4 (&acc)[2][2][4][2], const Unit& u, int wr, int wc, int fr, int fq) const {
;     ...
;             for (int m = 0; m < 4; ++m) { const int r = r0 + ai * 128 + m * 16; const bool ok = r < u.aux1; const int pid = ok ? list[u.aux0 + r] : 0;
;                 v4u w;
;                 { const f32x4 a0 = acc[ai][0][m][0] * sc, a1 = acc[ai][0][m][1] * sc, a2 = acc[ai][1][m][0] * sc, a3 = acc[ai][1][m][1] * sc;
;                   w.x = (unsigned)__builtin_amdgcn_cvt_pk_fp8_f32(a0[2], a0[3], __builtin_amdgcn_cvt_pk_fp8_f32(a0[0], a0[1], 0, false), true);
;                   w.y = (unsigned)__builtin_amdgcn_cvt_pk_fp8_f32(a1[2], a1[3], __builtin_amdgcn_cvt_pk_fp8_f32(a1[0], a1[1], 0, false), true);
;                   w.z = (unsigned)__builtin_amdgcn_cvt_pk_fp8_f32(a2[2], a2[3], __builtin_amdgcn_cvt_pk_fp8_f32(a2[0], a2[1], 0, false), true);
;                   w.w = (unsigned)__builtin_amdgcn_cvt_pk_fp8_f32(a3[2], a3[3], __builtin_amdgcn_cvt_pk_fp8_f32(a3[0], a3[1], 0, false), true); }
;                 w = lane_xpose(w, lane);
;                 if (ok) *(v4u*)(Y + (size_t)pid * 1024 + col0) = w; }
.LBB0_1364:
	s_or_b64 exec, exec, s[8:9]
	s_waitcnt lgkmcnt(0)
	v_mov_b64_e32 v[52:53], v[62:63]
	v_mov_b32_e32 v68, v163
	v_cvt_pk_fp8_f32 v68, v52, v53
	v_mov_b32_e32 v52, v163
	v_mov_b64_e32 v[62:63], v[78:79]
	v_mov_b64_e32 v[66:67], v[74:75]
	v_cvt_pk_fp8_f32 v52, v58, v59
	v_mov_b32_e32 v53, v163
	v_mov_b32_e32 v58, v163
	v_cvt_pk_fp8_f32 v53, v62, v63
	v_cvt_pk_fp8_f32 v58, v66, v67
	v_mov_b64_e32 v[50:51], v[64:65]
	v_mov_b64_e32 v[56:57], v[60:61]
	v_mov_b64_e32 v[60:61], v[80:81]
	v_mov_b64_e32 v[64:65], v[76:77]
	v_cvt_pk_fp8_f32 v68, v50, v51 op_sel:[0,0,1]
	v_cvt_pk_fp8_f32 v52, v56, v57 op_sel:[0,0,1]
	v_cvt_pk_fp8_f32 v53, v60, v61 op_sel:[0,0,1]
	v_cvt_pk_fp8_f32 v58, v64, v65 op_sel:[0,0,1]
	ds_bpermute_b32 v50, v144, v68
	ds_bpermute_b32 v51, v144, v52
	ds_bpermute_b32 v52, v144, v53
	ds_bpermute_b32 v53, v144, v58
	s_and_saveexec_b64 s[8:9], vcc
	s_cbranch_execz .LBB0_1366
	v_lshl_add_u64 v[54:55], s[12:13], 0, v[54:55]
	v_lshl_add_u64 v[54:55], v[54:55], 0, v[162:163]
	s_waitcnt lgkmcnt(0)
	global_store_dwordx4 v[54:55], v[50:53], off

;     __device__ __forceinline__ void operator()(const f32x4 (&acc)[2][2][4][2], const Unit& u, int wr, int wc, int fr, int fq) const {
;     ...
;             for (int m = 0; m < 4; ++m) { const int r = r0 + ai * 128 + m * 16; const bool ok = r < u.aux1; const int pid = ok ? list[u.aux0 + r] : 0;
;                 v4u w;
;                 { const f32x4 a0 = acc[ai][0][m][0] * sc, a1 = acc[ai][0][m][1] * sc, a2 = acc[ai][1][m][0] * sc, a3 = acc[ai][1][m][1] * sc;
;                   w.x = (unsigned)__builtin_amdgcn_cvt_pk_fp8_f32(a0[2], a0[3], __builtin_amdgcn_cvt_pk_fp8_f32(a0[0], a0[1], 0, false), true);
;                   w.y = (unsigned)__builtin_amdgcn_cvt_pk_fp8_f32(a1[2], a1[3], __builtin_amdgcn_cvt_pk_fp8_f32(a1[0], a1[1], 0, false), true);
;                   w.z = (unsigned)__builtin_amdgcn_cvt_pk_fp8_f32(a2[2], a2[3], __builtin_amdgcn_cvt_pk_fp8_f32(a2[0], a2[1], 0, false), true);
;                   w.w = (unsigned)__builtin_amdgcn_cvt_pk_fp8_f32(a3[2], a3[3], __builtin_amdgcn_cvt_pk_fp8_f32(a3[0], a3[1], 0, false), true); }
;                 w = lane_xpose(w, lane);
;                 if (ok) *(v4u*)(Y + (size_t)pid * 1024 + col0) = w; }
.LBB0_1368:
	s_or_b64 exec, exec, s[8:9]
	v_mov_b32_e32 v52, v163
	v_cvt_pk_fp8_f32 v52, v38, v39
	v_mov_b32_e32 v39, v163
	v_mov_b32_e32 v38, v163
	v_cvt_pk_fp8_f32 v39, v46, v47
	v_mov_b32_e32 v46, v163
	v_cvt_pk_fp8_f32 v38, v34, v35
	v_cvt_pk_fp8_f32 v46, v42, v43
	v_cvt_pk_fp8_f32 v52, v40, v41 op_sel:[0,0,1]
	v_cvt_pk_fp8_f32 v38, v36, v37 op_sel:[0,0,1]
	v_cvt_pk_fp8_f32 v39, v48, v49 op_sel:[0,0,1]
	v_cvt_pk_fp8_f32 v46, v44, v45 op_sel:[0,0,1]
	ds_bpermute_b32 v34, v144, v52
	ds_bpermute_b32 v35, v144, v38
	ds_bpermute_b32 v36, v144, v39
	ds_bpermute_b32 v37, v144, v46
	s_and_saveexec_b64 s[8:9], vcc
	s_cbranch_execz .LBB0_1370
	v_lshl_add_u64 v[38:39], s[12:13], 0, v[50:51]
	v_lshl_add_u64 v[38:39], v[38:39], 0, v[162:163]
	s_waitcnt lgkmcnt(0)
	global_store_dwordx4 v[38:39], v[34:37], off

;     __device__ __forceinline__ void operator()(const f32x4 (&acc)[2][2][4][2], const Unit& u, int wr, int wc, int fr, int fq) const {
;     ...
;             for (int m = 0; m < 4; ++m) { const int r = r0 + ai * 128 + m * 16; const bool ok = r < u.aux1; const int pid = ok ? list[u.aux0 + r] : 0;
;                 v4u w;
;                 { const f32x4 a0 = acc[ai][0][m][0] * sc, a1 = acc[ai][0][m][1] * sc, a2 = acc[ai][1][m][0] * sc, a3 = acc[ai][1][m][1] * sc;
;                   w.x = (unsigned)__builtin_amdgcn_cvt_pk_fp8_f32(a0[2], a0[3], __builtin_amdgcn_cvt_pk_fp8_f32(a0[0], a0[1], 0, false), true);
;                   w.y = (unsigned)__builtin_amdgcn_cvt_pk_fp8_f32(a1[2], a1[3], __builtin_amdgcn_cvt_pk_fp8_f32(a1[0], a1[1], 0, false), true);
;                   w.z = (unsigned)__builtin_amdgcn_cvt_pk_fp8_f32(a2[2], a2[3], __builtin_amdgcn_cvt_pk_fp8_f32(a2[0], a2[1], 0, false), true);
;                   w.w = (unsigned)__builtin_amdgcn_cvt_pk_fp8_f32(a3[2], a3[3], __builtin_amdgcn_cvt_pk_fp8_f32(a3[0], a3[1], 0, false), true); }
;                 w = lane_xpose(w, lane);
;                 if (ok) *(v4u*)(Y + (size_t)pid * 1024 + col0) = w; }
.LBB0_1372:
	s_or_b64 exec, exec, s[8:9]
	v_mov_b32_e32 v36, v163
	v_cvt_pk_fp8_f32 v36, v22, v23
	v_mov_b32_e32 v23, v163
	v_mov_b32_e32 v22, v163
	v_cvt_pk_fp8_f32 v23, v30, v31
	v_mov_b32_e32 v30, v163
	v_cvt_pk_fp8_f32 v22, v18, v19
	v_cvt_pk_fp8_f32 v30, v26, v27
	v_cvt_pk_fp8_f32 v36, v24, v25 op_sel:[0,0,1]
	v_cvt_pk_fp8_f32 v22, v20, v21 op_sel:[0,0,1]
	v_cvt_pk_fp8_f32 v23, v32, v33 op_sel:[0,0,1]
	v_cvt_pk_fp8_f32 v30, v28, v29 op_sel:[0,0,1]
	ds_bpermute_b32 v18, v144, v36
	ds_bpermute_b32 v19, v144, v22
	ds_bpermute_b32 v20, v144, v23
	ds_bpermute_b32 v21, v144, v30
	s_and_saveexec_b64 s[8:9], vcc
	s_cbranch_execz .LBB0_1374
	v_lshl_add_u64 v[22:23], s[12:13], 0, v[34:35]
	v_lshl_add_u64 v[22:23], v[22:23], 0, v[162:163]
	s_waitcnt lgkmcnt(0)
	global_store_dwordx4 v[22:23], v[18:21], off

;     __device__ __forceinline__ void operator()(const f32x4 (&acc)[2][2][4][2], const Unit& u, int wr, int wc, int fr, int fq) const {
;     ...
;             for (int m = 0; m < 4; ++m) { const int r = r0 + ai * 128 + m * 16; const bool ok = r < u.aux1; const int pid = ok ? list[u.aux0 + r] : 0;
;                 v4u w;
;                 { const f32x4 a0 = acc[ai][0][m][0] * sc, a1 = acc[ai][0][m][1] * sc, a2 = acc[ai][1][m][0] * sc, a3 = acc[ai][1][m][1] * sc;
;                   w.x = (unsigned)__builtin_amdgcn_cvt_pk_fp8_f32(a0[2], a0[3], __builtin_amdgcn_cvt_pk_fp8_f32(a0[0], a0[1], 0, false), true);
;                   w.y = (unsigned)__builtin_amdgcn_cvt_pk_fp8_f32(a1[2], a1[3], __builtin_amdgcn_cvt_pk_fp8_f32(a1[0], a1[1], 0, false), true);
;                   w.z = (unsigned)__builtin_amdgcn_cvt_pk_fp8_f32(a2[2], a2[3], __builtin_amdgcn_cvt_pk_fp8_f32(a2[0], a2[1], 0, false), true);
;                   w.w = (unsigned)__builtin_amdgcn_cvt_pk_fp8_f32(a3[2], a3[3], __builtin_amdgcn_cvt_pk_fp8_f32(a3[0], a3[1], 0, false), true); }
;                 w = lane_xpose(w, lane);
;                 if (ok) *(v4u*)(Y + (size_t)pid * 1024 + col0) = w; }
.LBB0_1376:
	s_or_b64 exec, exec, s[8:9]
	v_mov_b32_e32 v20, v163
	v_cvt_pk_fp8_f32 v20, v10, v11
	v_mov_b32_e32 v10, v163
	v_cvt_pk_fp8_f32 v10, v6, v7
	v_mov_b32_e32 v6, v163
	v_mov_b32_e32 v7, v163
	v_cvt_pk_fp8_f32 v6, v14, v15
	v_cvt_pk_fp8_f32 v7, v2, v3
	v_cvt_pk_fp8_f32 v20, v12, v13 op_sel:[0,0,1]
	v_cvt_pk_fp8_f32 v10, v8, v9 op_sel:[0,0,1]
	v_cvt_pk_fp8_f32 v6, v16, v17 op_sel:[0,0,1]
	v_cvt_pk_fp8_f32 v7, v4, v5 op_sel:[0,0,1]
	ds_bpermute_b32 v2, v144, v20
	ds_bpermute_b32 v3, v144, v10
	ds_bpermute_b32 v4, v144, v6
	ds_bpermute_b32 v5, v144, v7
	s_and_saveexec_b64 s[8:9], vcc
	s_cbranch_execz .LBB0_1378
	v_lshl_add_u64 v[6:7], s[12:13], 0, v[18:19]
	v_lshl_add_u64 v[6:7], v[6:7], 0, v[162:163]
	s_waitcnt lgkmcnt(0)
	global_store_dwordx4 v[6:7], v[2:5], off
